# start-stagger with 8 delay levels (max ~4.5 us) instead of 16 in A8/F2; otherwise v040
# speedup vs baseline: 1.0044x; 1.0027x over previous
.LBB0_1186:
	s_cmp_ge_i32 s36, s28
	s_cselect_b64 s[6:7], -1, 0
	s_and_b64 s[4:5], s[6:7], s[4:5]
	s_andn2_b64 vcc, exec, s[4:5]
	s_cbranch_vccnz .LBB0_1206
	s_waitcnt lgkmcnt(0)
	v_readlane_b32 s8, v254, 0
	s_nop 3
	s_cmp_lt_u32 s8, 16
	s_cbranch_scc1 .Lstg_a8_done
	s_mul_i32 s8, s8, 5
	s_and_b32 s8, s8, 7
	s_cmp_eq_u32 s8, 0
	s_cbranch_scc1 .Lstg_a8_done

.LBB0_1758:
	s_cmp_ge_i32 s36, s28
	s_cselect_b64 s[8:9], -1, 0
	s_and_b64 s[4:5], s[8:9], s[4:5]
	s_andn2_b64 vcc, exec, s[4:5]
	s_cbranch_vccnz .LBB0_1782
	v_readlane_b32 s6, v254, 0
	s_nop 3
	s_cmp_lt_u32 s6, 16
	s_cbranch_scc1 .Lstg_f2_done
	s_mul_i32 s6, s6, 5
	s_and_b32 s6, s6, 7
	s_cmp_eq_u32 s6, 0
	s_cbranch_scc1 .Lstg_f2_done
